# attention GQA+MLA loops: back-edge pointer bumps and slot selects moved ahead of the step barrier (loop-edge rotation), on top of v040
# speedup vs baseline: 1.0005x; 1.0005x over previous
.LBB0_900:
	s_or_b64 exec, exec, s[20:21]
	s_add_i32 s12, s50, 0x3000
	s_cmpk_lg_i32 s50, 0x6000
	s_cselect_b32 s12, s12, 0
	s_add_i32 s20, s13, 0x2000
	s_cmpk_lg_i32 s13, 0x4000
	s_cselect_b32 s49, s20, 0
	s_add_i32 s20, s49, s48
	s_mov_b32 s21, m0
	s_mov_b32 m0, s20
	s_nop 0
	global_load_lds_dwordx4 v[16:17], off
	s_mov_b32 m0, s21
	v_add_f32_e32 v2, v232, v2
	v_add_f32_e32 v232, v2, v110
	v_mfma_f32_32x32x16_bf16 v[18:33], v[138:141], v[146:149], v[18:33]
	v_exp_f32_e32 v66, v66
	v_exp_f32_e32 v67, v67
	v_exp_f32_e32 v68, v68
	v_exp_f32_e32 v69, v69
	s_waitcnt lgkmcnt(12)
	v_mfma_f32_32x32x16_bf16 v[34:49], v[138:141], v[142:145], v[34:49]
	v_exp_f32_e32 v70, v70
	v_exp_f32_e32 v71, v71
	v_exp_f32_e32 v72, v72
	v_exp_f32_e32 v73, v73
	v_add_u32_e32 v2, s12, v253
	ds_read_b128 v[186:189], v2
	ds_read_b128 v[178:181], v2 offset:512
	s_waitcnt lgkmcnt(12)
	v_mfma_f32_32x32x16_bf16 v[18:33], v[12:15], v[98:101], v[18:33]
	v_exp_f32_e32 v74, v74
	v_exp_f32_e32 v75, v75
	v_exp_f32_e32 v76, v76
	v_exp_f32_e32 v77, v77
	ds_read_b128 v[182:185], v2 offset:2048
	ds_read_b128 v[174:177], v2 offset:2560
	s_waitcnt lgkmcnt(12)
	v_mfma_f32_32x32x16_bf16 v[34:49], v[12:15], v[102:105], v[34:49]
	v_exp_f32_e32 v78, v78
	v_exp_f32_e32 v79, v79
	v_exp_f32_e32 v80, v80
	v_exp_f32_e32 v81, v81
	ds_read_b128 v[170:173], v2 offset:4096
	ds_read_b128 v[166:169], v2 offset:4608
	s_waitcnt lgkmcnt(12)
	v_mfma_f32_32x32x16_bf16 v[18:33], v[8:11], v[106:109], v[18:33]
	v_exp_f32_e32 v50, v50
	v_exp_f32_e32 v51, v51
	v_exp_f32_e32 v52, v52
	v_exp_f32_e32 v53, v53
	ds_read_b128 v[162:165], v2 offset:6144
	ds_read_b128 v[150:153], v2 offset:6656
	s_waitcnt lgkmcnt(12)
	v_mfma_f32_32x32x16_bf16 v[34:49], v[8:11], v[82:85], v[34:49]
	v_exp_f32_e32 v54, v54
	v_exp_f32_e32 v55, v55
	v_exp_f32_e32 v56, v56
	v_exp_f32_e32 v57, v57
	ds_read_b128 v[146:149], v2 offset:8192
	ds_read_b128 v[142:145], v2 offset:8704
	s_waitcnt lgkmcnt(12)
	v_mfma_f32_32x32x16_bf16 v[18:33], v[4:7], v[86:89], v[18:33]
	v_exp_f32_e32 v58, v58
	v_exp_f32_e32 v59, v59
	v_exp_f32_e32 v60, v60
	v_exp_f32_e32 v61, v61
	ds_read_b128 v[158:161], v2 offset:10240
	ds_read_b128 v[154:157], v2 offset:10752
	s_waitcnt lgkmcnt(12)
	v_mfma_f32_32x32x16_bf16 v[34:49], v[4:7], v[90:93], v[34:49]
	v_exp_f32_e32 v62, v62
	v_exp_f32_e32 v63, v63
	v_exp_f32_e32 v64, v64
	v_exp_f32_e32 v65, v65
	s_add_i32 s20, s12, 0x3000
	s_cmpk_lg_i32 s12, 0x6000
	s_cselect_b32 s50, s20, 0
	s_add_i32 s20, s49, 0x2000
	s_cmpk_lg_i32 s49, 0x4000
	s_cselect_b32 s20, s20, 0
	s_add_i32 s21, s25, 2
	s_add_u32 s10, s10, 0x30000
	s_addc_u32 s11, s11, 0
	v_lshl_add_u64 v[16:17], v[16:17], 0, s[82:83]
	s_cmp_ge_u32 s21, s77
	s_waitcnt vmcnt(3) lgkmcnt(0)
	s_barrier
	s_cbranch_scc1 .LBB0_919
	s_mov_b32 s25, s21
	s_mov_b32 s21, s13
	s_mov_b32 s13, s20
	s_branch .LBB0_896

.LBB0_910:
	s_mov_b32 s40, s13
	s_mov_b32 s8, s24
	s_mov_b32 s9, s39
	v_add_u32_e32 v2, s11, v242
	ds_read_b64_tr_b16 v[172:173], v2 offset:24576
	ds_read_b64_tr_b16 v[174:175], v2 offset:25088
	v_add_f32_e32 v68, v52, v53
	v_add_f32_e32 v68, v54, v68
	v_add_f32_e32 v68, v55, v68
	v_add_f32_e32 v68, v56, v68
	v_add_f32_e32 v68, v57, v68
	v_cvt_pk_bf16_f32 v128, v52, v53
	v_cvt_pk_bf16_f32 v129, v54, v55
	s_waitcnt lgkmcnt(9)
	v_mfma_f32_32x32x16_bf16 v[84:99], v[160:163], v[112:115], 0
	ds_read_b64_tr_b16 v[52:53], v2 offset:28672
	ds_read_b64_tr_b16 v[54:55], v2 offset:29184
	v_add_f32_e32 v68, v58, v68
	v_add_f32_e32 v68, v59, v68
	v_add_f32_e32 v68, v60, v68
	v_add_f32_e32 v116, v61, v68
	v_cvt_pk_bf16_f32 v130, v56, v57
	v_cvt_pk_bf16_f32 v131, v58, v59
	s_waitcnt lgkmcnt(10)
	v_mfma_f32_32x32x16_bf16 v[68:83], v[152:155], v[112:115], 0
	ds_read_b64_tr_b16 v[56:57], v2 offset:25600
	ds_read_b64_tr_b16 v[58:59], v2 offset:26112
	v_add_f32_e32 v116, v62, v116
	v_add_f32_e32 v116, v63, v116
	v_add_f32_e32 v116, v64, v116
	v_add_f32_e32 v116, v65, v116
	v_cvt_pk_bf16_f32 v124, v60, v61
	v_cvt_pk_bf16_f32 v125, v62, v63
	s_waitcnt lgkmcnt(11)
	v_mfma_f32_32x32x16_bf16 v[84:99], v[156:159], v[108:111], v[84:99]
	ds_read_b64_tr_b16 v[60:61], v2 offset:29696
	ds_read_b64_tr_b16 v[62:63], v2 offset:30208
	v_add_f32_e32 v116, v66, v116
	v_add_f32_e32 v116, v67, v116
	v_add_f32_e32 v116, v36, v116
	v_add_f32_e32 v116, v37, v116
	v_cvt_pk_bf16_f32 v126, v64, v65
	v_cvt_pk_bf16_f32 v127, v66, v67
	s_waitcnt lgkmcnt(12)
	v_mfma_f32_32x32x16_bf16 v[68:83], v[148:151], v[108:111], v[68:83]
	ds_read_b64_tr_b16 v[64:65], v2 offset:26624
	ds_read_b64_tr_b16 v[66:67], v2 offset:27136
	v_add_f32_e32 v116, v38, v116
	v_add_f32_e32 v116, v39, v116
	v_add_f32_e32 v116, v40, v116
	v_add_f32_e32 v116, v41, v116
	v_cvt_pk_bf16_f32 v120, v36, v37
	v_cvt_pk_bf16_f32 v121, v38, v39
	s_waitcnt lgkmcnt(13)
	v_mfma_f32_32x32x16_bf16 v[84:99], v[144:147], v[104:107], v[84:99]
	ds_read_b64_tr_b16 v[36:37], v2 offset:30720
	ds_read_b64_tr_b16 v[38:39], v2 offset:31232
	v_add_f32_e32 v116, v42, v116
	v_add_f32_e32 v116, v43, v116
	v_add_f32_e32 v116, v44, v116
	v_add_f32_e32 v116, v45, v116
	v_cvt_pk_bf16_f32 v122, v40, v41
	v_cvt_pk_bf16_f32 v123, v42, v43
	s_waitcnt lgkmcnt(14)
	v_mfma_f32_32x32x16_bf16 v[68:83], v[140:143], v[104:107], v[68:83]
	ds_read_b64_tr_b16 v[40:41], v2 offset:27648
	ds_read_b64_tr_b16 v[42:43], v2 offset:28160
	v_add_f32_e32 v116, v46, v116
	v_add_f32_e32 v116, v47, v116
	v_add_f32_e32 v116, v48, v116
	s_waitcnt lgkmcnt(14)
	v_mfma_f32_32x32x16_bf16 v[84:99], v[136:139], v[100:103], v[84:99]
	v_add_f32_e32 v136, v49, v116
	v_cvt_pk_bf16_f32 v116, v44, v45
	v_cvt_pk_bf16_f32 v117, v46, v47
	ds_read_b64_tr_b16 v[44:45], v2 offset:31744
	ds_read_b64_tr_b16 v[46:47], v2 offset:32256
	v_add_f32_e32 v2, v50, v136
	v_add_f32_e32 v2, v51, v2
	v_add_f32_e32 v2, 0, v2
	v_cvt_pk_bf16_f32 v118, v48, v49
	v_cvt_pk_bf16_f32 v119, v50, v51
	v_mfma_f32_32x32x16_bf16 v[68:83], v[132:135], v[100:103], v[68:83]
	v_lshl_add_u64 v[48:49], v[170:171], 0, s[94:95]
	s_add_i32 s11, s12, s36
	s_mov_b32 s12, m0
	s_mov_b32 m0, s11
	s_nop 0
	global_load_lds_dwordx4 v[48:49], off
	s_mov_b32 m0, s12
	v_lshl_add_u64 v[48:49], v[168:169], 0, s[94:95]
	s_add_i32 s11, s13, s38
	s_mov_b32 s12, m0
	s_mov_b32 m0, s11
	s_nop 0
	global_load_lds_dwordx4 v[48:49], off
	s_mov_b32 m0, s12
	v_add_f32_e32 v2, v176, v2
	s_waitcnt lgkmcnt(14)
	v_mfma_f32_32x32x16_bf16 v[4:19], v[128:131], v[172:175], v[4:19]
	v_exp_f32_e32 v84, v84
	v_exp_f32_e32 v85, v85
	v_exp_f32_e32 v86, v86
	v_exp_f32_e32 v87, v87
	s_waitcnt lgkmcnt(12)
	v_mfma_f32_32x32x16_bf16 v[20:35], v[128:131], v[52:55], v[20:35]
	v_exp_f32_e32 v88, v88
	v_exp_f32_e32 v89, v89
	v_exp_f32_e32 v90, v90
	v_exp_f32_e32 v91, v91
	v_add_u32_e32 v52, s91, v253
	ds_read_b128 v[48:51], v52
	ds_read_b128 v[136:139], v52 offset:512
	s_waitcnt lgkmcnt(12)
	v_mfma_f32_32x32x16_bf16 v[4:19], v[124:127], v[56:59], v[4:19]
	v_exp_f32_e32 v92, v92
	v_exp_f32_e32 v93, v93
	v_exp_f32_e32 v94, v94
	v_exp_f32_e32 v95, v95
	ds_read_b128 v[140:143], v52 offset:2048
	ds_read_b128 v[144:147], v52 offset:2560
	s_waitcnt lgkmcnt(12)
	v_mfma_f32_32x32x16_bf16 v[20:35], v[124:127], v[60:63], v[20:35]
	v_exp_f32_e32 v96, v96
	v_exp_f32_e32 v97, v97
	v_exp_f32_e32 v98, v98
	v_exp_f32_e32 v99, v99
	ds_read_b128 v[148:151], v52 offset:4096
	ds_read_b128 v[152:155], v52 offset:4608
	s_waitcnt lgkmcnt(12)
	v_mfma_f32_32x32x16_bf16 v[4:19], v[120:123], v[64:67], v[4:19]
	v_exp_f32_e32 v68, v68
	v_exp_f32_e32 v69, v69
	v_exp_f32_e32 v70, v70
	v_exp_f32_e32 v71, v71
	ds_read_b128 v[156:159], v52 offset:6144
	ds_read_b128 v[132:135], v52 offset:6656
	s_waitcnt lgkmcnt(12)
	v_mfma_f32_32x32x16_bf16 v[20:35], v[120:123], v[36:39], v[20:35]
	v_exp_f32_e32 v72, v72
	v_exp_f32_e32 v73, v73
	v_exp_f32_e32 v74, v74
	v_exp_f32_e32 v75, v75
	s_waitcnt lgkmcnt(10)
	v_mfma_f32_32x32x16_bf16 v[4:19], v[116:119], v[40:43], v[4:19]
	v_exp_f32_e32 v76, v76
	v_exp_f32_e32 v77, v77
	v_exp_f32_e32 v78, v78
	v_exp_f32_e32 v79, v79
	s_waitcnt lgkmcnt(8)
	v_mfma_f32_32x32x16_bf16 v[20:35], v[116:119], v[44:47], v[20:35]
	v_exp_f32_e32 v80, v80
	v_exp_f32_e32 v81, v81
	v_exp_f32_e32 v82, v82
	v_exp_f32_e32 v83, v83
	s_add_i32 s11, s91, 0x2000
	s_cmpk_lg_i32 s91, 0x4000
	s_waitcnt vmcnt(2) lgkmcnt(0)
	s_barrier
	s_cselect_b32 s12, s11, 0
	s_add_i32 s11, s13, 0x2000
	s_cmpk_lg_i32 s13, 0x4000
	s_cselect_b32 s39, s11, 0
	v_add_u32_e32 v172, s9, v242
	ds_read_b64_tr_b16 v[160:161], v172 offset:24576
	ds_read_b64_tr_b16 v[162:163], v172 offset:25088
	s_waitcnt lgkmcnt(9)
	v_mfma_f32_32x32x16_bf16 v[52:67], v[48:51], v[112:115], 0
	v_add_f32_e32 v36, v84, v85
	v_add_f32_e32 v36, v86, v36
	v_add_f32_e32 v36, v87, v36
	v_add_f32_e32 v36, v88, v36
	v_add_f32_e32 v36, v89, v36
	v_cvt_pk_bf16_f32 v128, v84, v85
	v_cvt_pk_bf16_f32 v129, v86, v87
	ds_read_b64_tr_b16 v[84:85], v172 offset:28672
	ds_read_b64_tr_b16 v[86:87], v172 offset:29184
	v_add_f32_e32 v36, v90, v36
	v_add_f32_e32 v36, v91, v36
	v_add_f32_e32 v36, v92, v36
	v_add_f32_e32 v116, v93, v36
	s_waitcnt lgkmcnt(10)
	v_mfma_f32_32x32x16_bf16 v[36:51], v[136:139], v[112:115], 0
	v_cvt_pk_bf16_f32 v130, v88, v89
	v_cvt_pk_bf16_f32 v131, v90, v91
	ds_read_b64_tr_b16 v[88:89], v172 offset:25600
	ds_read_b64_tr_b16 v[90:91], v172 offset:26112
	s_waitcnt lgkmcnt(11)
	v_mfma_f32_32x32x16_bf16 v[52:67], v[140:143], v[108:111], v[52:67]
	v_add_f32_e32 v116, v94, v116
	v_add_f32_e32 v116, v95, v116
	v_add_f32_e32 v116, v96, v116
	v_add_f32_e32 v116, v97, v116
	v_cvt_pk_bf16_f32 v124, v92, v93
	v_cvt_pk_bf16_f32 v125, v94, v95
	ds_read_b64_tr_b16 v[92:93], v172 offset:29696
	ds_read_b64_tr_b16 v[94:95], v172 offset:30208
	s_waitcnt lgkmcnt(12)
	v_mfma_f32_32x32x16_bf16 v[36:51], v[144:147], v[108:111], v[36:51]
	v_add_f32_e32 v116, v98, v116
	v_add_f32_e32 v116, v99, v116
	v_add_f32_e32 v116, v68, v116
	v_add_f32_e32 v116, v69, v116
	v_cvt_pk_bf16_f32 v126, v96, v97
	v_cvt_pk_bf16_f32 v127, v98, v99
	ds_read_b64_tr_b16 v[96:97], v172 offset:26624
	ds_read_b64_tr_b16 v[98:99], v172 offset:27136
	s_waitcnt lgkmcnt(13)
	v_mfma_f32_32x32x16_bf16 v[52:67], v[148:151], v[104:107], v[52:67]
	v_add_f32_e32 v116, v70, v116
	v_add_f32_e32 v116, v71, v116
	v_add_f32_e32 v116, v72, v116
	v_add_f32_e32 v116, v73, v116
	v_cvt_pk_bf16_f32 v120, v68, v69
	v_cvt_pk_bf16_f32 v121, v70, v71
	ds_read_b64_tr_b16 v[68:69], v172 offset:30720
	ds_read_b64_tr_b16 v[70:71], v172 offset:31232
	s_waitcnt lgkmcnt(14)
	v_mfma_f32_32x32x16_bf16 v[36:51], v[152:155], v[104:107], v[36:51]
	v_add_f32_e32 v116, v74, v116
	v_add_f32_e32 v116, v75, v116
	v_add_f32_e32 v116, v76, v116
	v_add_f32_e32 v116, v77, v116
	v_cvt_pk_bf16_f32 v122, v72, v73
	v_cvt_pk_bf16_f32 v123, v74, v75
	ds_read_b64_tr_b16 v[72:73], v172 offset:27648
	ds_read_b64_tr_b16 v[74:75], v172 offset:28160
	s_waitcnt lgkmcnt(14)
	v_mfma_f32_32x32x16_bf16 v[52:67], v[156:159], v[100:103], v[52:67]
	v_add_f32_e32 v116, v78, v116
	v_add_f32_e32 v116, v79, v116
	v_add_f32_e32 v116, v80, v116
	v_add_f32_e32 v136, v81, v116
	v_cvt_pk_bf16_f32 v116, v76, v77
	v_cvt_pk_bf16_f32 v117, v78, v79
	ds_read_b64_tr_b16 v[76:77], v172 offset:31744
	ds_read_b64_tr_b16 v[78:79], v172 offset:32256
	v_mfma_f32_32x32x16_bf16 v[36:51], v[132:135], v[100:103], v[36:51]
	v_add_f32_e32 v118, v82, v136
	v_add_f32_e32 v118, v83, v118
	v_add_f32_e32 v132, 0, v118
	v_cvt_pk_bf16_f32 v118, v80, v81
	v_cvt_pk_bf16_f32 v119, v82, v83
	s_add_i32 s9, s91, s36
	s_mov_b32 s11, m0
	s_mov_b32 m0, s9
	s_nop 0
	global_load_lds_dwordx4 v[170:171], off
	s_mov_b32 m0, s11
	s_add_i32 s9, s39, s38
	s_mov_b32 s11, m0
	s_mov_b32 m0, s9
	s_nop 0
	global_load_lds_dwordx4 v[168:169], off
	s_mov_b32 m0, s11
	v_add_f32_e32 v176, v2, v132
	s_waitcnt lgkmcnt(14)
	v_mfma_f32_32x32x16_bf16 v[4:19], v[128:131], v[160:163], v[4:19]
	v_exp_f32_e32 v52, v52
	v_exp_f32_e32 v53, v53
	v_exp_f32_e32 v54, v54
	v_exp_f32_e32 v55, v55
	s_waitcnt lgkmcnt(12)
	v_mfma_f32_32x32x16_bf16 v[20:35], v[128:131], v[84:87], v[20:35]
	v_exp_f32_e32 v56, v56
	v_exp_f32_e32 v57, v57
	v_exp_f32_e32 v58, v58
	v_exp_f32_e32 v59, v59
	v_add_u32_e32 v2, s12, v253
	ds_read_b128 v[160:163], v2
	ds_read_b128 v[152:155], v2 offset:512
	s_waitcnt lgkmcnt(12)
	v_mfma_f32_32x32x16_bf16 v[4:19], v[124:127], v[88:91], v[4:19]
	v_exp_f32_e32 v60, v60
	v_exp_f32_e32 v61, v61
	v_exp_f32_e32 v62, v62
	v_exp_f32_e32 v63, v63
	ds_read_b128 v[156:159], v2 offset:2048
	ds_read_b128 v[148:151], v2 offset:2560
	s_waitcnt lgkmcnt(12)
	v_mfma_f32_32x32x16_bf16 v[20:35], v[124:127], v[92:95], v[20:35]
	v_exp_f32_e32 v64, v64
	v_exp_f32_e32 v65, v65
	v_exp_f32_e32 v66, v66
	v_exp_f32_e32 v67, v67
	ds_read_b128 v[144:147], v2 offset:4096
	ds_read_b128 v[140:143], v2 offset:4608
	s_waitcnt lgkmcnt(12)
	v_mfma_f32_32x32x16_bf16 v[4:19], v[120:123], v[96:99], v[4:19]
	v_exp_f32_e32 v36, v36
	v_exp_f32_e32 v37, v37
	v_exp_f32_e32 v38, v38
	v_exp_f32_e32 v39, v39
	ds_read_b128 v[136:139], v2 offset:6144
	ds_read_b128 v[132:135], v2 offset:6656
	s_waitcnt lgkmcnt(12)
	v_mfma_f32_32x32x16_bf16 v[20:35], v[120:123], v[68:71], v[20:35]
	v_exp_f32_e32 v40, v40
	v_exp_f32_e32 v41, v41
	v_exp_f32_e32 v42, v42
	v_exp_f32_e32 v43, v43
	s_waitcnt lgkmcnt(10)
	v_mfma_f32_32x32x16_bf16 v[4:19], v[116:119], v[72:75], v[4:19]
	v_exp_f32_e32 v44, v44
	v_exp_f32_e32 v45, v45
	v_exp_f32_e32 v46, v46
	v_exp_f32_e32 v47, v47
	s_waitcnt lgkmcnt(8)
	v_mfma_f32_32x32x16_bf16 v[20:35], v[116:119], v[76:79], v[20:35]
	v_exp_f32_e32 v48, v48
	v_exp_f32_e32 v49, v49
	v_exp_f32_e32 v50, v50
	v_exp_f32_e32 v51, v51
	s_add_i32 s9, s12, 0x2000
	s_cmpk_lg_i32 s12, 0x4000
	s_cselect_b32 s91, s9, 0
	s_add_i32 s9, s39, 0x2000
	s_cmpk_lg_i32 s39, 0x4000
	s_cselect_b32 s13, s9, 0
	s_add_i32 s24, s24, 2
	v_lshl_add_u64 v[168:169], v[168:169], 0, s[92:93]
	v_lshl_add_u64 v[170:171], v[170:171], 0, s[92:93]
	s_mov_b32 s11, s40
	s_cmp_ge_u32 s24, s77
	s_waitcnt vmcnt(2) lgkmcnt(0)
	s_barrier
	s_cbranch_scc0 .LBB0_910
	s_add_i32 s24, s8, -3
	s_ashr_i32 s11, s10, 31
	s_add_i32 s8, s24, 1
	s_cmp_ge_u32 s8, s77
	s_cbranch_scc0 .LBB0_962
